# s14 + P4 non-critical roles throttled (scan s_sleep 8 per step, converter s_sleep 40 per two items)
# speedup vs baseline: 1.0070x; 1.0070x over previous
; __device__ __forceinline__ void item8_load(const float* W, int N, int k0, int n0, int lane, f32x4 (&rg)[16]) {
; #pragma unroll
;     for (int i = 0; i < 16; ++i) rg[i] = __builtin_nontemporal_load((const f32x4*)(W + (size_t)(k0 + 8 * i + (lane >> 3)) * N + n0 + 4 * (lane & 7)));
; }
.LBB0_472:
	s_sleep 40
	s_cmp_gt_i32 s2, 0xe9ff
	s_mov_b64 s[4:5], -1
	s_cbranch_scc1 .LBB0_471
	s_add_i32 s8, s2, s3
	s_cmp_lt_i32 s8, 0xea00
	s_cselect_b64 s[6:7], -1, 0
	s_cmp_gt_i32 s8, 0xe9ff
	s_cselect_b64 s[4:5], -1, 0
	s_and_b64 vcc, exec, s[4:5]
	s_cbranch_vccnz .LBB0_475
	s_ashr_i32 s9, s8, 31
	s_lshr_b32 s9, s9, 21
	s_add_i32 s9, s8, s9
	s_and_b32 s14, s9, 0xf800
	s_sub_i32 s18, s8, s14
	s_ashr_i32 s14, s9, 11
	s_ashr_i32 s15, s14, 31
	s_lshl_b64 s[14:15], s[14:15], 25
	s_add_u32 s9, s66, s14
	s_sext_i32_i16 s14, s18
	s_addc_u32 s19, s67, s15
	s_bfe_u32 s14, s14, 0x70018
	s_add_i32 s14, s18, s14
	s_sext_i32_i16 s15, s14
	s_and_b32 s14, s14, 0xff80
	s_sub_i32 s14, s18, s14
	s_sext_i32_i16 s14, s14
	s_and_b32 s15, s15, 0xffffff80
	s_lshl_b32 s14, s14, 5
	s_waitcnt vmcnt(4)
	v_or_b32_e32 v122, s15, v134
	s_ashr_i32 s15, s14, 31
	s_lshl_b64 s[14:15], s[14:15], 2
	v_ashrrev_i32_e32 v123, 31, v122
	s_add_u32 s14, s9, s14
	v_lshlrev_b64 v[66:67], 14, v[122:123]
	v_or_b32_e32 v68, 8, v122
	v_or_b32_e32 v74, 16, v122
	v_or_b32_e32 v76, 24, v122
	v_or_b32_e32 v82, 32, v122
	v_or_b32_e32 v84, 40, v122
	v_or_b32_e32 v90, 48, v122
	v_or_b32_e32 v92, 56, v122
	v_or_b32_e32 v98, 64, v122
	v_or_b32_e32 v100, 0x48, v122
	v_or_b32_e32 v106, 0x50, v122
	v_or_b32_e32 v108, 0x58, v122
	v_or_b32_e32 v114, 0x60, v122
	v_or_b32_e32 v116, 0x68, v122
	v_or_b32_e32 v126, 0x70, v122
	v_or_b32_e32 v122, 0x78, v122
	s_addc_u32 s15, s19, s15
	v_ashrrev_i32_e32 v69, 31, v68
	v_ashrrev_i32_e32 v75, 31, v74
	v_ashrrev_i32_e32 v77, 31, v76
	v_ashrrev_i32_e32 v83, 31, v82
	v_ashrrev_i32_e32 v85, 31, v84
	v_ashrrev_i32_e32 v91, 31, v90
	v_ashrrev_i32_e32 v93, 31, v92
	v_ashrrev_i32_e32 v99, 31, v98
	v_ashrrev_i32_e32 v101, 31, v100
	v_ashrrev_i32_e32 v107, 31, v106
	v_ashrrev_i32_e32 v109, 31, v108
	v_ashrrev_i32_e32 v115, 31, v114
	v_ashrrev_i32_e32 v117, 31, v116
	v_ashrrev_i32_e32 v127, 31, v126
	v_ashrrev_i32_e32 v123, 31, v122
	v_lshl_add_u64 v[124:125], v[130:131], 2, s[14:15]
	v_lshlrev_b64 v[68:69], 14, v[68:69]
	v_lshlrev_b64 v[74:75], 14, v[74:75]
	v_lshlrev_b64 v[76:77], 14, v[76:77]
	v_lshlrev_b64 v[82:83], 14, v[82:83]
	v_lshlrev_b64 v[84:85], 14, v[84:85]
	v_lshlrev_b64 v[90:91], 14, v[90:91]
	v_lshlrev_b64 v[92:93], 14, v[92:93]
	v_lshlrev_b64 v[98:99], 14, v[98:99]
	v_lshlrev_b64 v[100:101], 14, v[100:101]
	v_lshlrev_b64 v[106:107], 14, v[106:107]
	v_lshlrev_b64 v[108:109], 14, v[108:109]
	v_lshlrev_b64 v[114:115], 14, v[114:115]
	v_lshlrev_b64 v[116:117], 14, v[116:117]
	v_lshlrev_b64 v[126:127], 14, v[126:127]
	v_lshlrev_b64 v[122:123], 14, v[122:123]
	v_lshl_add_u64 v[66:67], v[124:125], 0, v[66:67]
	v_lshl_add_u64 v[68:69], v[124:125], 0, v[68:69]
	v_lshl_add_u64 v[74:75], v[124:125], 0, v[74:75]
	v_lshl_add_u64 v[76:77], v[124:125], 0, v[76:77]
	v_lshl_add_u64 v[82:83], v[124:125], 0, v[82:83]
	v_lshl_add_u64 v[84:85], v[124:125], 0, v[84:85]
	v_lshl_add_u64 v[90:91], v[124:125], 0, v[90:91]
	v_lshl_add_u64 v[92:93], v[124:125], 0, v[92:93]
	v_lshl_add_u64 v[98:99], v[124:125], 0, v[98:99]
	v_lshl_add_u64 v[100:101], v[124:125], 0, v[100:101]
	v_lshl_add_u64 v[106:107], v[124:125], 0, v[106:107]
	v_lshl_add_u64 v[108:109], v[124:125], 0, v[108:109]
	v_lshl_add_u64 v[114:115], v[124:125], 0, v[114:115]
	v_lshl_add_u64 v[116:117], v[124:125], 0, v[116:117]
	v_lshl_add_u64 v[126:127], v[124:125], 0, v[126:127]
	v_lshl_add_u64 v[122:123], v[124:125], 0, v[122:123]
	global_load_dwordx4 v[70:73], v[66:67], off nt
	s_nop 0
	global_load_dwordx4 v[66:69], v[68:69], off nt
	s_nop 0
	global_load_dwordx4 v[78:81], v[74:75], off nt
	s_nop 0
	global_load_dwordx4 v[74:77], v[76:77], off nt
	s_nop 0
	global_load_dwordx4 v[86:89], v[82:83], off nt
	s_nop 0
	global_load_dwordx4 v[82:85], v[84:85], off nt
	s_nop 0
	global_load_dwordx4 v[94:97], v[90:91], off nt
	s_nop 0
	global_load_dwordx4 v[90:93], v[92:93], off nt
	s_nop 0
	global_load_dwordx4 v[102:105], v[98:99], off nt
	s_nop 0
	global_load_dwordx4 v[98:101], v[100:101], off nt
	s_nop 0
	global_load_dwordx4 v[110:113], v[106:107], off nt
	s_nop 0
	global_load_dwordx4 v[106:109], v[108:109], off nt
	s_nop 0
	global_load_dwordx4 v[118:121], v[114:115], off nt
	s_nop 0
	global_load_dwordx4 v[114:117], v[116:117], off nt
	s_nop 0
	global_load_dwordx4 v[126:129], v[126:127], off nt
	s_nop 0
	global_load_dwordx4 v[122:125], v[122:123], off nt

; #define LAS __attribute__((address_space(3)))
; __global__ void __launch_bounds__(NTHREADS, 2) fwd(Args args) {
;     ...
;                 for (int n = 0; n < 68; ++n) {
;                     const int c = dir ? (n < 4 ? 3 - n : 71 - n) : n;
;                     const LAS unsigned char* base = lds + (n & 1) * GBUF;
;                     if (c >= 4) {
.LBB0_483:
	s_sleep 8
	s_cmp_gt_u32 s8, 3
	s_cselect_b32 s6, 0x47, 3
	s_add_i32 s9, s6, s2
	s_and_b64 s[6:7], s[4:5], exec
	s_cselect_b32 s6, s8, s9
	s_cmp_gt_i32 s6, 3
	s_mov_b64 s[6:7], -1
	s_cbranch_scc1 .LBB0_485
	s_mov_b64 s[6:7], 0
